# v14 + kernel prologue: all kernarg s_loads issued together (one round trip instead of five); stage B gate loads issued before the workgroup barrier
# speedup vs baseline: 1.0011x; 1.0011x over previous
; __global__ void __launch_bounds__(NWAVES * 64, 2) mk_fwd(Args args) {
;     ...
;     F.lds = (LAS unsigned char*)lds;
;     F.MISC = (volatile LAS unsigned*)(F.lds + MISC_OFF);
;     F.tid = threadIdx.x; F.lane = F.tid & 63; F.wave = __builtin_amdgcn_readfirstlane(F.tid >> 6);
;     F.G = gridDim.x; { const int bx = blockIdx.x; F.vcu = (F.G % 8 == 0) ? (bx % 8) * (F.G / 8) + bx / 8 : bx; }
;     unsigned char* ws = args.ws;
;     F.ctl = (gu32*)(ws + WS_CTL);
;     F.x = args.in[0]; F.c = args.in[1]; F.ada_w = args.in[2]; F.ada_b = args.in[3]; F.norm_mix_g = args.in[4]; F.w_in = args.in[5]; F.b_gates = args.in[6];
;     F.conv_w = args.in[7]; F.conv_b = args.in[8]; F.gmlp_norm_g = args.in[9]; F.gmlp_w = args.in[10]; F.gmlp_b = args.in[11]; F.mlstm_norm_g = args.in[12];
;     F.w_out = args.in[13]; F.norm_ffn_g = args.in[14]; F.wq = args.in[15]; F.keys1 = args.in[16]; F.keys2 = args.in[17]; F.e_down = args.in[18]; F.e_up = args.in[19]; F.final_g = args.in[20];
;     F.out = args.out;
;     F.MODP = (float*)(ws + WS_MODP); F.MODF = (float*)(ws + WS_MODF); F.GATES = (float*)(ws + WS_GATES); F.SUMM = (float*)(ws + WS_SUMM); F.MTAB = (float*)(ws + WS_MTAB);
;     F.NST = (float*)(ws + WS_NST); F.PG = (float*)(ws + WS_PG); F.IDX = (int*)(ws + WS_IDX);
;     F.WIN = (bf16*)(ws + WS_WIN); F.WOUT = (bf16*)(ws + WS_WOUT); F.WQ = (bf16*)(ws + WS_WQ); F.HA = (bf16*)(ws + WS_HA); F.PROJ = (bf16*)(ws + WS_PROJ); F.QB = (bf16*)(ws + WS_PROJ);
;     F.STATE = (bf16*)(ws + WS_STATE); F.VT = (bf16*)(ws + WS_VT); F.ED = ws + WS_ED; F.EU = ws + WS_EU; F.XB = (bf16*)(ws + WS_XB); F.SD = (float*)(ws + WS_SD); F.SU = (float*)(ws + WS_SU);
;     F.H2Q = ws + WS_HA; F.WQ8 = ws + WS_WQ; F.CMAXQ = (float*)(ws + WS_BQP); F.SWQ = (float*)(ws + WS_BIASQ);
;     F.YQ = ws + WS_PROJ + 64 * MiB; F.WO8 = ws + WS_WOUT; F.SY = (float*)(ws + WS_SSQP); F.CMAXO = (float*)(ws + WS_CMAXP + 768 * 1024); F.SWO = (float*)(ws + WS_BQP + 256 * 1024);
;     F.H1Q = ws + WS_STATE;
;     F.SW = (float*)(ws + WS_SW); F.CMAXP = (float*)(ws + WS_CMAXP); F.SA = (float*)(ws + WS_SA);
;     F.SSQP = (float*)(ws + WS_SSQP); F.BQP = (float*)(ws + WS_BQP); F.BIASQ = (float*)(ws + WS_BIASQ); F.X1B = (bf16*)(ws + WS_STATE);
;     F.QC = (bf16*)args.out; F.KC = (bf16*)args.out + (size_t)M * 1024;
;     for (int u = F.tid; u < (LDS_BYTES - LDSCTL_OFF) / 4; u += NWAVES * 64) ((LAS unsigned*)(F.lds + LDSCTL_OFF))[u] = 0u;
_Z6mk_fwd4Args:
	s_load_dwordx2 s[8:9], s[0:1], 0xb0
	s_load_dwordx4 s[4:7], s[0:1], 0xa0
	s_load_dwordx4 s[84:87], s[0:1], 0xb8
	s_load_dword s88, s[0:1], 0xc8
	s_load_dwordx8 s[76:83], s[0:1], 0x80
	s_load_dwordx16 s[60:75], s[0:1], 0x0
	s_load_dwordx16 s[32:47], s[0:1], 0x40
	s_mov_b32 s58, s2
	v_readfirstlane_b32 s2, v0
	s_waitcnt lgkmcnt(0)
	v_writelane_b32 v252, s4, 0
	s_nop 1
	v_writelane_b32 v252, s5, 1
	v_writelane_b32 v252, s6, 2
	v_writelane_b32 v252, s7, 3
	v_writelane_b32 v252, s84, 4
	s_nop 1
	v_writelane_b32 v252, s85, 5
	v_writelane_b32 v252, s86, 6
	v_writelane_b32 v252, s87, 7
	s_mov_b32 s4, s88
	v_writelane_b32 v252, s2, 8
	s_add_u32 s2, s0, 0xc8
	s_addc_u32 s3, s1, 0
	v_writelane_b32 v252, s2, 9
	s_nop 1
	v_writelane_b32 v252, s3, 10
	s_waitcnt lgkmcnt(0)
	s_and_b32 s2, s4, 7
	v_writelane_b32 v252, s4, 11
	s_cmp_lg_u32 s2, 0
	v_writelane_b32 v252, s58, 12
	s_cbranch_scc1 .LBB0_2
	s_mov_b32 s2, s88
	s_ashr_i32 s3, s58, 31
	s_lshr_b32 s3, s3, 29
	s_add_i32 s3, s58, s3
	s_and_b32 s4, s3, -8
	s_waitcnt lgkmcnt(0)
	s_ashr_i32 s2, s2, 3
	s_sub_i32 s4, s58, s4
	s_mul_i32 s2, s2, s4
	s_ashr_i32 s3, s3, 3
	s_add_i32 s2, s2, s3
	v_writelane_b32 v252, s2, 12
.LBB0_2:
	s_movk_i32 s2, 0x80
	v_writelane_b32 v252, s8, 13
	v_cmp_gt_u32_e32 vcc, s2, v0
	s_nop 0
	v_writelane_b32 v252, s9, 14
	s_and_saveexec_b64 s[2:3], vcc
	v_lshl_add_u32 v1, v0, 2, 0
	v_add_u32_e32 v1, 0x27e00, v1
	v_mov_b32_e32 v2, 0
	ds_write_b32 v1, v2
	s_or_b64 exec, exec, s[2:3]
	s_mov_b64 s[4:5], s[32:33]
	s_mov_b64 s[6:7], s[34:35]
	s_mov_b64 s[8:9], s[36:37]
	s_mov_b64 s[10:11], s[38:39]
	s_mov_b64 s[12:13], s[40:41]
	s_mov_b64 s[14:15], s[42:43]
	s_mov_b64 s[16:17], s[44:45]
	s_mov_b64 s[18:19], s[46:47]
	v_cmp_eq_u32_e32 vcc, 0, v0
	s_waitcnt lgkmcnt(0)
	s_barrier
	v_writelane_b32 v252, s4, 15
	s_nop 1
	v_writelane_b32 v252, s5, 16
	v_writelane_b32 v252, s6, 17
	v_writelane_b32 v252, s7, 18
	v_writelane_b32 v252, s8, 19
	v_writelane_b32 v252, s9, 20
	v_writelane_b32 v252, s10, 21
	v_writelane_b32 v252, s11, 22
	v_writelane_b32 v252, s12, 23
	v_writelane_b32 v252, s13, 24
	v_writelane_b32 v252, s14, 25
	v_writelane_b32 v252, s15, 26
	v_writelane_b32 v252, s16, 27
	v_writelane_b32 v252, s17, 28
	v_writelane_b32 v252, s18, 29
	v_writelane_b32 v252, s19, 30
	s_nop 0
	v_readlane_b32 s0, v252, 4
	v_readlane_b32 s1, v252, 5
	s_sub_i32 s0, s1, s0
	s_cmp_gt_i32 s0, 1
	s_cselect_b64 s[4:5], -1, 0
	v_readlane_b32 s2, v252, 6
	v_readlane_b32 s3, v252, 7
	v_writelane_b32 v252, s4, 31
	s_mulk_i32 s2, 0xd80
	s_nop 0
	v_writelane_b32 v252, s5, 32
	s_nop 0
	v_readlane_b32 s4, v252, 13
	v_readlane_b32 s5, v252, 14
	s_add_u32 s1, s4, 0x4000
	v_writelane_b32 v252, s1, 33
	s_addc_u32 s1, s5, 0
	v_writelane_b32 v252, s1, 34
	s_ashr_i32 s3, s2, 31
	v_writelane_b32 v252, s2, 35
	s_cmp_lt_i32 s0, 2
	s_mov_b32 s0, 0
	v_writelane_b32 v252, s3, 36
	v_writelane_b32 v252, s0, 37
	s_cbranch_scc1 .LBB0_9
	s_getreg_b32 s0, hwreg(HW_REG_XCC_ID, 0, 4)
	s_and_b32 s0, s0, 15
	v_writelane_b32 v252, s0, 37
	s_and_saveexec_b64 s[0:1], vcc
	s_cbranch_execz .LBB0_8
	s_mov_b64 s[2:3], exec
	v_mbcnt_lo_u32_b32 v1, s2, 0
	v_mbcnt_hi_u32_b32 v1, s3, v1
	v_cmp_eq_u32_e32 vcc, 0, v1
	s_and_b64 s[4:5], exec, vcc
	s_mov_b64 exec, s[4:5]
	s_cbranch_execz .LBB0_8
	v_readlane_b32 s4, v252, 35
	v_readlane_b32 s5, v252, 36
	s_lshl_b64 s[4:5], s[4:5], 2
	v_readlane_b32 s6, v252, 33
	s_add_u32 s4, s6, s4
	v_readlane_b32 s6, v252, 34
	s_addc_u32 s5, s6, s5
	v_readlane_b32 s6, v252, 37
	s_lshl_b32 s6, s6, 8
	s_bcnt1_i32_b64 s2, s[2:3]
	v_mov_b32_e32 v1, s6
	v_mov_b32_e32 v2, s2
	global_atomic_add v1, v2, s[4:5] offset:1024

; #define LAS __attribute__((address_space(3)))
; #define P9B_LOAD(P) do { _Pragma("unroll") for (int u = 0; u < 2; ++u) { const int tl_ = F.wave * 8 + 2 * (P) + u; _Pragma("unroll") for (int h = 0; h < 2; ++h) { const unsigned e = IDX16[tl_ * 128 + 64 * h + slot]; \
;                 sdn[u][h] = F.SD[e]; sun[u][h] = F.SU[e]; pgn[u][h] = F.PG[(size_t)(tb + tl_) * NSEL + 64 * h + lane]; } } } while (0)
; DI void p9v2_phase(Frame& F) {
;     ...
;         __builtin_amdgcn_s_setprio(0);
;         __syncthreads();
;         LAS int* PI = (LAS int*)F.lds;
; #pragma unroll
;         for (int j = 0; j < 8; ++j) { const int tl = F.wave * 8 + j; PI[tl * 128 + 8 * c8 + g] = P[j][0]; PI[tl * 128 + 64 + 8 * c8 + g] = P[j][1]; }
; #pragma unroll
;         for (int i = 0; i < 4; ++i) { const int c = tid + 512 * i; GF[c] = F.MODF[MOD_GF + c]; FG[c] = F.final_g[c]; }
;         LAS float* SSQL = (LAS float*)(F.lds + P9_SSQ); LAS signed char* CQ = (LAS signed char*)(F.lds + P9_CQ); LAS float* CT = (LAS float*)(F.lds + P9_CT); LAS int* CSQ = (LAS int*)(F.lds + P9_CSQ);
;         {
;             const int slot = 8 * (lane & 7) + (lane >> 3);
;             float sdn[2][2], sun[2][2], pgn[2][2];
;     ...
;             P9B_LOAD(0);
.LBB0_1307:
	s_setprio 0
	v_add_u32_e32 v2, s63, v162
	global_load_dword v30, v[132:133], off
	global_load_dword v31, v[134:135], off
	global_load_dword v32, v[134:135], off offset:2048
	global_load_dword v33, v[136:137], off
	global_load_dword v34, v[138:139], off
	global_load_dword v35, v[140:141], off
	global_load_dword v36, v[142:143], off
	s_barrier
	ds_read_u16 v4, v2
	ds_read_u16 v5, v2 offset:128
	global_load_dword v37, v[144:145], off
	s_lshl_b64 s[44:45], s[42:43], 9
	v_lshl_add_u64 v[2:3], v[150:151], 0, s[44:45]
	s_waitcnt lgkmcnt(1)
	v_lshlrev_b32_e32 v24, 2, v4
	v_add_u32_e32 v4, s66, v162
	ds_read_u16 v22, v4
	ds_read_u16 v4, v4 offset:128
	global_load_dword v28, v[2:3], off
	global_load_dword v26, v[2:3], off offset:256
	s_lshl_b64 s[14:15], s[14:15], 9
	s_waitcnt lgkmcnt(2)
	v_lshlrev_b32_e32 v5, 2, v5
	v_lshl_add_u64 v[2:3], v[150:151], 0, s[14:15]
	s_waitcnt lgkmcnt(1)
	v_lshlrev_b32_e32 v38, 2, v22
	s_waitcnt lgkmcnt(0)
	v_lshlrev_b32_e32 v39, 2, v4
	global_load_dword v23, v38, s[24:25]
	global_load_dword v22, v39, s[24:25]
	global_load_dword v4, v24, s[20:21]
	global_load_dword v29, v24, s[24:25]
	global_load_dword v27, v5, s[24:25]
	s_nop 0
	global_load_dword v5, v5, s[20:21]
	s_nop 0
	global_load_dword v24, v[2:3], off offset:256
	global_load_dword v25, v[2:3], off
	s_nop 0
	global_load_dword v2, v38, s[20:21]
	global_load_dword v3, v39, s[20:21]
	ds_write2st64_b32 v183, v6, v7 offset1:1
	ds_write2st64_b32 v183, v8, v9 offset0:2 offset1:3
	ds_write2st64_b32 v183, v10, v11 offset0:4 offset1:5
	ds_write2st64_b32 v183, v12, v13 offset0:6 offset1:7
	ds_write2st64_b32 v183, v14, v15 offset0:8 offset1:9
	ds_write2st64_b32 v183, v16, v17 offset0:10 offset1:11
	ds_write2st64_b32 v183, v18, v19 offset0:12 offset1:13
	ds_write2st64_b32 v183, v20, v21 offset0:14 offset1:15
	s_mov_b32 s23, 0
	v_mov_b32_e32 v6, v187
	s_waitcnt vmcnt(16)
	ds_write2st64_b32 v180, v30, v33 offset0:128 offset1:136
	ds_write2st64_b32 v180, v31, v32 offset0:160 offset1:168
	s_waitcnt vmcnt(13)
	ds_write2st64_b32 v180, v34, v36 offset0:144 offset1:152
	s_waitcnt vmcnt(12)
	ds_write2st64_b32 v180, v35, v37 offset0:176 offset1:184
	s_waitcnt vmcnt(9)
	v_mov_b32_e32 v13, v23
	s_waitcnt vmcnt(8)
	v_mov_b32_e32 v14, v22
	v_mov_b32_e32 v9, v28
	v_mov_b32_e32 v10, v26
	s_waitcnt vmcnt(5)
	v_mov_b32_e32 v8, v27
	v_mov_b32_e32 v7, v29
	s_waitcnt vmcnt(3)
	v_mov_b32_e32 v12, v24
	s_waitcnt vmcnt(2)
	v_mov_b32_e32 v11, v25
	s_branch .LBB0_1309
